# P9 expert-down epilogue: lanes regrouped with ds_bpermute so each quad of lanes stores 32 contiguous bytes (no LDS staging, no barriers); rest as v30
# speedup vs baseline: 1.0106x; 1.0030x over previous
.LBB0_996:
	s_lshl_b32 s21, s23, 10
	s_and_b32 s21, s21, 0x400
	s_nop 15
	s_nop 15
	v_add_u32_e32 v2, s21, v205
	ds_read_b128 v[12:15], v2
	ds_read_b128 v[16:19], v2 offset:16
	ds_read_b128 v[4:7], v2 offset:512
	ds_read_b128 v[8:11], v2 offset:528
	v_and_b32_e32 v36, 63, v0
	v_and_b32_e32 v37, 3, v36
	v_lshrrev_b32_e32 v38, 2, v36
	v_lshl_or_b32 v40, v37, 4, v38
	v_lshlrev_b32_e32 v40, 2, v40
	v_and_b32_e32 v41, 0xfffffff0, v221
	v_or_b32_e32 v41, v41, v38
	v_and_b32_e32 v42, 0xffffffe7, v209
	v_lshl_or_b32 v42, v37, 3, v42
	v_lshl_or_b32 v45, v41, 10, v42
	s_lshl_b32 s3, s22, 8
	s_and_b32 s3, s3, 0x300
	s_lshl_b32 s40, s69, 18
	s_add_i32 s3, s3, s40
	s_add_u32 s40, s14, s3
	s_addc_u32 s41, s15, 0
	s_waitcnt lgkmcnt(0)
	v_pk_add_f32 v[20:21], v[80:81], v[12:13]
	v_pk_add_f32 v[22:23], v[88:89], v[16:17]
	v_mov_b32_e32 v28, v3
	v_mov_b32_e32 v29, v3
	v_pk_add_f32 v[24:25], v[82:83], v[14:15]
	v_pk_add_f32 v[26:27], v[90:91], v[18:19]
	v_cvt_pk_fp8_f32 v28, v20, v21
	v_cvt_pk_fp8_f32 v29, v22, v23
	v_cvt_pk_fp8_f32 v28, v24, v25 op_sel:[0,0,1]
	v_cvt_pk_fp8_f32 v29, v26, v27 op_sel:[0,0,1]
	v_pk_add_f32 v[20:21], v[144:145], v[4:5]
	v_pk_add_f32 v[22:23], v[154:155], v[8:9]
	v_mov_b32_e32 v30, v3
	v_mov_b32_e32 v31, v3
	v_pk_add_f32 v[24:25], v[146:147], v[6:7]
	v_pk_add_f32 v[26:27], v[156:157], v[10:11]
	v_cvt_pk_fp8_f32 v30, v20, v21
	v_cvt_pk_fp8_f32 v31, v22, v23
	v_cvt_pk_fp8_f32 v30, v24, v25 op_sel:[0,0,1]
	v_cvt_pk_fp8_f32 v31, v26, v27 op_sel:[0,0,1]
	ds_bpermute_b32 v32, v40, v28
	ds_bpermute_b32 v33, v40, v29
	ds_bpermute_b32 v34, v40, v30
	ds_bpermute_b32 v35, v40, v31
	v_pk_add_f32 v[20:21], v[96:97], v[12:13]
	v_pk_add_f32 v[22:23], v[104:105], v[16:17]
	v_mov_b32_e32 v56, v3
	v_mov_b32_e32 v57, v3
	v_pk_add_f32 v[24:25], v[98:99], v[14:15]
	v_pk_add_f32 v[26:27], v[106:107], v[18:19]
	v_cvt_pk_fp8_f32 v56, v20, v21
	v_cvt_pk_fp8_f32 v57, v22, v23
	v_cvt_pk_fp8_f32 v56, v24, v25 op_sel:[0,0,1]
	v_cvt_pk_fp8_f32 v57, v26, v27 op_sel:[0,0,1]
	v_pk_add_f32 v[20:21], v[158:159], v[4:5]
	v_pk_add_f32 v[22:23], v[162:163], v[8:9]
	v_mov_b32_e32 v58, v3
	v_mov_b32_e32 v59, v3
	v_pk_add_f32 v[24:25], v[160:161], v[6:7]
	v_pk_add_f32 v[26:27], v[164:165], v[10:11]
	v_cvt_pk_fp8_f32 v58, v20, v21
	v_cvt_pk_fp8_f32 v59, v22, v23
	v_cvt_pk_fp8_f32 v58, v24, v25 op_sel:[0,0,1]
	v_cvt_pk_fp8_f32 v59, v26, v27 op_sel:[0,0,1]
	ds_bpermute_b32 v48, v40, v56
	ds_bpermute_b32 v49, v40, v57
	ds_bpermute_b32 v50, v40, v58
	ds_bpermute_b32 v51, v40, v59
	s_waitcnt lgkmcnt(4)
	global_store_dwordx2 v45, v[32:33], s[40:41]
	global_store_dwordx2 v45, v[34:35], s[40:41] offset:128
	s_add_u32 s40, s40, 0x4000
	s_addc_u32 s41, s41, 0
	v_pk_add_f32 v[20:21], v[112:113], v[12:13]
	v_pk_add_f32 v[22:23], v[120:121], v[16:17]
	v_mov_b32_e32 v28, v3
	v_mov_b32_e32 v29, v3
	v_pk_add_f32 v[24:25], v[114:115], v[14:15]
	v_pk_add_f32 v[26:27], v[122:123], v[18:19]
	v_cvt_pk_fp8_f32 v28, v20, v21
	v_cvt_pk_fp8_f32 v29, v22, v23
	v_cvt_pk_fp8_f32 v28, v24, v25 op_sel:[0,0,1]
	v_cvt_pk_fp8_f32 v29, v26, v27 op_sel:[0,0,1]
	v_pk_add_f32 v[20:21], v[166:167], v[4:5]
	v_pk_add_f32 v[22:23], v[170:171], v[8:9]
	v_mov_b32_e32 v30, v3
	v_mov_b32_e32 v31, v3
	v_pk_add_f32 v[24:25], v[168:169], v[6:7]
	v_pk_add_f32 v[26:27], v[172:173], v[10:11]
	v_cvt_pk_fp8_f32 v30, v20, v21
	v_cvt_pk_fp8_f32 v31, v22, v23
	v_cvt_pk_fp8_f32 v30, v24, v25 op_sel:[0,0,1]
	v_cvt_pk_fp8_f32 v31, v26, v27 op_sel:[0,0,1]
	ds_bpermute_b32 v32, v40, v28
	ds_bpermute_b32 v33, v40, v29
	ds_bpermute_b32 v34, v40, v30
	ds_bpermute_b32 v35, v40, v31
	s_waitcnt lgkmcnt(4)
	global_store_dwordx2 v45, v[48:49], s[40:41]
	global_store_dwordx2 v45, v[50:51], s[40:41] offset:128
	s_add_u32 s40, s40, 0x4000
	s_addc_u32 s41, s41, 0
	v_pk_add_f32 v[20:21], v[128:129], v[12:13]
	v_pk_add_f32 v[22:23], v[132:133], v[16:17]
	v_mov_b32_e32 v56, v3
	v_mov_b32_e32 v57, v3
	v_pk_add_f32 v[24:25], v[130:131], v[14:15]
	v_pk_add_f32 v[26:27], v[134:135], v[18:19]
	v_cvt_pk_fp8_f32 v56, v20, v21
	v_cvt_pk_fp8_f32 v57, v22, v23
	v_cvt_pk_fp8_f32 v56, v24, v25 op_sel:[0,0,1]
	v_cvt_pk_fp8_f32 v57, v26, v27 op_sel:[0,0,1]
	v_pk_add_f32 v[20:21], v[174:175], v[4:5]
	v_pk_add_f32 v[22:23], v[182:183], v[8:9]
	v_mov_b32_e32 v58, v3
	v_mov_b32_e32 v59, v3
	v_pk_add_f32 v[24:25], v[176:177], v[6:7]
	v_pk_add_f32 v[26:27], v[184:185], v[10:11]
	v_cvt_pk_fp8_f32 v58, v20, v21
	v_cvt_pk_fp8_f32 v59, v22, v23
	v_cvt_pk_fp8_f32 v58, v24, v25 op_sel:[0,0,1]
	v_cvt_pk_fp8_f32 v59, v26, v27 op_sel:[0,0,1]
	ds_bpermute_b32 v48, v40, v56
	ds_bpermute_b32 v49, v40, v57
	ds_bpermute_b32 v50, v40, v58
	ds_bpermute_b32 v51, v40, v59
	s_waitcnt lgkmcnt(4)
	global_store_dwordx2 v45, v[32:33], s[40:41]
	global_store_dwordx2 v45, v[34:35], s[40:41] offset:128
	s_add_u32 s40, s40, 0x4000
	s_addc_u32 s41, s41, 0
	v_pk_add_f32 v[20:21], v[68:69], v[12:13]
	v_pk_add_f32 v[22:23], v[72:73], v[16:17]
	v_mov_b32_e32 v28, v3
	v_mov_b32_e32 v29, v3
	v_pk_add_f32 v[24:25], v[70:71], v[14:15]
	v_pk_add_f32 v[26:27], v[74:75], v[18:19]
	v_cvt_pk_fp8_f32 v28, v20, v21
	v_cvt_pk_fp8_f32 v29, v22, v23
	v_cvt_pk_fp8_f32 v28, v24, v25 op_sel:[0,0,1]
	v_cvt_pk_fp8_f32 v29, v26, v27 op_sel:[0,0,1]
	v_pk_add_f32 v[20:21], v[124:125], v[4:5]
	v_pk_add_f32 v[22:23], v[136:137], v[8:9]
	v_mov_b32_e32 v30, v3
	v_mov_b32_e32 v31, v3
	v_pk_add_f32 v[24:25], v[126:127], v[6:7]
	v_pk_add_f32 v[26:27], v[138:139], v[10:11]
	v_cvt_pk_fp8_f32 v30, v20, v21
	v_cvt_pk_fp8_f32 v31, v22, v23
	v_cvt_pk_fp8_f32 v30, v24, v25 op_sel:[0,0,1]
	v_cvt_pk_fp8_f32 v31, v26, v27 op_sel:[0,0,1]
	ds_bpermute_b32 v32, v40, v28
	ds_bpermute_b32 v33, v40, v29
	ds_bpermute_b32 v34, v40, v30
	ds_bpermute_b32 v35, v40, v31
	s_waitcnt lgkmcnt(4)
	global_store_dwordx2 v45, v[48:49], s[40:41]
	global_store_dwordx2 v45, v[50:51], s[40:41] offset:128
	s_add_u32 s40, s40, 0x14000
	s_addc_u32 s41, s41, 0
	v_pk_add_f32 v[20:21], v[76:77], v[12:13]
	v_pk_add_f32 v[22:23], v[84:85], v[16:17]
	v_mov_b32_e32 v56, v3
	v_mov_b32_e32 v57, v3
	v_pk_add_f32 v[24:25], v[78:79], v[14:15]
	v_pk_add_f32 v[26:27], v[86:87], v[18:19]
	v_cvt_pk_fp8_f32 v56, v20, v21
	v_cvt_pk_fp8_f32 v57, v22, v23
	v_cvt_pk_fp8_f32 v56, v24, v25 op_sel:[0,0,1]
	v_cvt_pk_fp8_f32 v57, v26, v27 op_sel:[0,0,1]
	v_pk_add_f32 v[20:21], v[140:141], v[4:5]
	v_pk_add_f32 v[22:23], v[150:151], v[8:9]
	v_mov_b32_e32 v58, v3
	v_mov_b32_e32 v59, v3
	v_pk_add_f32 v[24:25], v[142:143], v[6:7]
	v_pk_add_f32 v[26:27], v[152:153], v[10:11]
	v_cvt_pk_fp8_f32 v58, v20, v21
	v_cvt_pk_fp8_f32 v59, v22, v23
	v_cvt_pk_fp8_f32 v58, v24, v25 op_sel:[0,0,1]
	v_cvt_pk_fp8_f32 v59, v26, v27 op_sel:[0,0,1]
	ds_bpermute_b32 v48, v40, v56
	ds_bpermute_b32 v49, v40, v57
	ds_bpermute_b32 v50, v40, v58
	ds_bpermute_b32 v51, v40, v59
	s_waitcnt lgkmcnt(4)
	global_store_dwordx2 v45, v[32:33], s[40:41]
	global_store_dwordx2 v45, v[34:35], s[40:41] offset:128
	s_add_u32 s40, s40, 0x4000
	s_addc_u32 s41, s41, 0
	v_pk_add_f32 v[20:21], v[92:93], v[12:13]
	v_pk_add_f32 v[22:23], v[100:101], v[16:17]
	v_mov_b32_e32 v28, v3
	v_mov_b32_e32 v29, v3
	v_pk_add_f32 v[24:25], v[94:95], v[14:15]
	v_pk_add_f32 v[26:27], v[102:103], v[18:19]
	v_cvt_pk_fp8_f32 v28, v20, v21
	v_cvt_pk_fp8_f32 v29, v22, v23
	v_cvt_pk_fp8_f32 v28, v24, v25 op_sel:[0,0,1]
	v_cvt_pk_fp8_f32 v29, v26, v27 op_sel:[0,0,1]
	v_pk_add_f32 v[20:21], v[178:179], v[4:5]
	v_pk_add_f32 v[22:23], v[186:187], v[8:9]
	v_mov_b32_e32 v30, v3
	v_mov_b32_e32 v31, v3
	v_pk_add_f32 v[24:25], v[180:181], v[6:7]
	v_pk_add_f32 v[26:27], v[188:189], v[10:11]
	v_cvt_pk_fp8_f32 v30, v20, v21
	v_cvt_pk_fp8_f32 v31, v22, v23
	v_cvt_pk_fp8_f32 v30, v24, v25 op_sel:[0,0,1]
	v_cvt_pk_fp8_f32 v31, v26, v27 op_sel:[0,0,1]
	ds_bpermute_b32 v32, v40, v28
	ds_bpermute_b32 v33, v40, v29
	ds_bpermute_b32 v34, v40, v30
	ds_bpermute_b32 v35, v40, v31
	s_waitcnt lgkmcnt(4)
	global_store_dwordx2 v45, v[48:49], s[40:41]
	global_store_dwordx2 v45, v[50:51], s[40:41] offset:128
	s_add_u32 s40, s40, 0x4000
	s_addc_u32 s41, s41, 0
	v_pk_add_f32 v[20:21], v[108:109], v[12:13]
	v_pk_add_f32 v[22:23], v[116:117], v[16:17]
	v_mov_b32_e32 v56, v3
	v_mov_b32_e32 v57, v3
	v_pk_add_f32 v[24:25], v[110:111], v[14:15]
	v_pk_add_f32 v[26:27], v[118:119], v[18:19]
	v_cvt_pk_fp8_f32 v56, v20, v21
	v_cvt_pk_fp8_f32 v57, v22, v23
	v_cvt_pk_fp8_f32 v56, v24, v25 op_sel:[0,0,1]
	v_cvt_pk_fp8_f32 v57, v26, v27 op_sel:[0,0,1]
	v_pk_add_f32 v[20:21], v[190:191], v[4:5]
	v_pk_add_f32 v[22:23], v[194:195], v[8:9]
	v_mov_b32_e32 v58, v3
	v_mov_b32_e32 v59, v3
	v_pk_add_f32 v[24:25], v[192:193], v[6:7]
	v_pk_add_f32 v[26:27], v[196:197], v[10:11]
	v_cvt_pk_fp8_f32 v58, v20, v21
	v_cvt_pk_fp8_f32 v59, v22, v23
	v_cvt_pk_fp8_f32 v58, v24, v25 op_sel:[0,0,1]
	v_cvt_pk_fp8_f32 v59, v26, v27 op_sel:[0,0,1]
	ds_bpermute_b32 v48, v40, v56
	ds_bpermute_b32 v49, v40, v57
	ds_bpermute_b32 v50, v40, v58
	ds_bpermute_b32 v51, v40, v59
	s_waitcnt lgkmcnt(4)
	global_store_dwordx2 v45, v[32:33], s[40:41]
	global_store_dwordx2 v45, v[34:35], s[40:41] offset:128
	s_add_u32 s40, s40, 0x4000
	s_addc_u32 s41, s41, 0
	s_waitcnt lgkmcnt(0)
	global_store_dwordx2 v45, v[48:49], s[40:41]
	global_store_dwordx2 v45, v[50:51], s[40:41] offset:128
	s_cmp_eq_u32 s23, s66
	s_mov_b64 s[22:23], -1
	s_cbranch_scc1 .LBB0_979
	s_andn2_b64 vcc, exec, s[8:9]
	s_cbranch_vccnz .LBB0_999
	s_ashr_i32 s22, s20, 2
	s_ashr_i32 s23, s22, 31
	s_lshl_b64 s[22:23], s[22:23], 12
	s_add_u32 s3, s52, s22
	s_addc_u32 s21, s53, s23
	s_lshl_b32 s22, s20, 10
	s_and_b32 s22, s22, 0xc00
	s_add_u32 s22, s3, s22
	s_addc_u32 s23, s21, 0
	s_lshl_b32 s3, s68, 10
	s_and_b32 s3, s3, 0x400
	s_add_i32 s3, s3, 0
	s_add_i32 m0, s3, 0x24000
	s_nop 0
	global_load_lds_dwordx4 v223, s[22:23]
